# RWKV helper block loop: dropped the vmcnt(8/1/0) ladder on the phi-copy block (it only waited for the acknowledgement of two just-issued stores; all loads are already drained at the block end) - stack
# baseline (speedup 1.0000x reference)
.LBB0_495:
	v_mov_b64_e32 v[56:57], v[32:33]
	v_mov_b64_e32 v[60:61], v[36:37]
	v_mov_b64_e32 v[48:49], v[24:25]
	v_mov_b64_e32 v[44:45], v[20:21]
	v_mov_b64_e32 v[40:41], v[16:17]
	v_mov_b64_e32 v[52:53], v[28:29]
	s_cmpk_gt_u32 s60, 0x7d
	v_mov_b64_e32 v[54:55], v[30:31]
	v_mov_b64_e32 v[58:59], v[34:35]
	v_mov_b64_e32 v[78:79], v[4:5]
	v_mov_b64_e32 v[80:81], v[62:63]
	v_mov_b64_e32 v[46:47], v[22:23]
	v_mov_b64_e32 v[42:43], v[18:19]
	v_mov_b64_e32 v[38:39], v[14:15]
	v_mov_b64_e32 v[50:51], v[26:27]
	s_cbranch_scc1 .LBB0_497
	v_lshl_add_u32 v40, s60, 15, v105
	v_or_b32_e32 v2, v40, v83
	v_readlane_b32 s80, v239, 44
	v_readlane_b32 s6, v239, 37
	v_readlane_b32 s8, v239, 33
	v_lshlrev_b64 v[44:45], 1, v[2:3]
	v_readlane_b32 s81, v239, 45
	v_readlane_b32 s7, v239, 38
	v_readlane_b32 s9, v239, 34
	v_lshl_add_u64 v[38:39], s[80:81], 0, v[44:45]
	v_lshl_add_u64 v[42:43], s[6:7], 0, v[44:45]
	v_lshl_add_u64 v[46:47], s[56:57], 0, v[44:45]
	v_lshl_add_u64 v[44:45], s[8:9], 0, v[44:45]
	v_add_u32_e32 v80, 0x4000, v40
	global_load_dwordx2 v[42:43], v[42:43], off
	v_mov_b32_e32 v41, v3
	global_load_dwordx2 v[50:51], v[44:45], off
	v_lshl_add_u64 v[44:45], v[2:3], 2, s[58:59]
	v_or_b32_e32 v2, v80, v83
	v_lshlrev_b64 v[52:53], 1, v[2:3]
	global_load_dwordx2 v[46:47], v[46:47], off
	v_lshl_add_u64 v[48:49], s[56:57], 0, v[52:53]
	global_load_dwordx4 v[54:57], v[44:45], off
	v_lshl_add_u64 v[44:45], v[40:41], 1, v[64:65]
	v_mov_b32_e32 v81, v3
	global_load_dwordx2 v[78:79], v[44:45], off
	v_lshl_add_u64 v[40:41], s[80:81], 0, v[52:53]
	global_load_dwordx2 v[48:49], v[48:49], off
	v_lshl_add_u64 v[44:45], s[6:7], 0, v[52:53]
	v_lshl_add_u64 v[52:53], s[8:9], 0, v[52:53]
	v_lshl_add_u64 v[58:59], v[2:3], 2, s[58:59]
	v_lshl_add_u64 v[80:81], v[80:81], 1, v[64:65]
	global_load_dwordx2 v[38:39], v[38:39], off
	s_nop 0
	global_load_dwordx2 v[40:41], v[40:41], off
	s_nop 0
	global_load_dwordx2 v[44:45], v[44:45], off
	s_nop 0
	global_load_dwordx2 v[52:53], v[52:53], off
	s_nop 0
	global_load_dwordx4 v[58:61], v[58:59], off
	s_nop 0
	global_load_dwordx2 v[80:81], v[80:81], off
